# attention phase: one static s_setprio 1 for waves 4-7 ahead of the item loop (reset after it)
# speedup vs baseline: 1.0017x; 1.0017x over previous
.LBB0_611:
	s_or_b64 exec, exec, s[0:1]
	s_cmpk_gt_i32 s12, 0x3ff
	s_waitcnt lgkmcnt(0)
	s_barrier
	s_cbranch_scc1 .LBB0_630
	v_readlane_b32 s72, v251, 11
	v_lshlrev_b32_e32 v2, 5, v0
	v_readlane_b32 s84, v251, 23
	v_readlane_b32 s85, v251, 24
	v_and_b32_e32 v7, 0x1e0, v2
	v_readlane_b32 s86, v251, 25
	v_readlane_b32 s87, v251, 26
	s_mov_b64 s[16:17], s[84:85]
	global_load_dwordx4 v[82:85], v7, s[16:17] offset:16
	global_load_dwordx4 v[86:89], v7, s[16:17]
	v_lshrrev_b32_e32 v3, 5, v1
	v_lshrrev_b32_e32 v6, 2, v0
	v_and_b32_e32 v7, 12, v200
	s_waitcnt vmcnt(15)
	v_bfe_u32 v11, v0, 2, 2
	v_and_b32_e32 v9, 15, v0
	v_and_b32_e32 v6, 12, v6
	v_bfe_u32 v10, v0, 6, 2
	v_or_b32_e32 v13, v7, v11
	v_bitop3_b32 v7, v3, v7, v11 bitop3:0x1e
	v_lshrrev_b32_e32 v154, 4, v0
	v_bitop3_b32 v10, v6, v9, v10 bitop3:0x36
	v_lshlrev_b32_e32 v163, 4, v7
	v_bitop3_b32 v7, v3, v13, 2 bitop3:0x36
	v_lshlrev_b32_e32 v8, 8, v154
	v_lshlrev_b32_e32 v6, 4, v10
	v_lshlrev_b32_e32 v164, 4, v7
	v_bitop3_b32 v7, v3, v13, 4 bitop3:0x36
	v_add3_u32 v157, 0, v6, v8
	v_lshrrev_b32_e32 v8, 3, v0
	v_lshlrev_b32_e32 v165, 4, v7
	v_bitop3_b32 v7, v3, v13, 6 bitop3:0x36
	s_waitcnt vmcnt(14)
	v_and_b32_e32 v16, 2, v8
	v_mbcnt_lo_u32_b32 v8, -1, 0
	v_lshlrev_b32_e32 v166, 4, v7
	v_bitop3_b32 v7, v3, v13, 8 bitop3:0x36
	v_mbcnt_hi_u32_b32 v8, -1, v8
	v_lshlrev_b32_e32 v167, 4, v7
	v_bitop3_b32 v7, v3, v13, 10 bitop3:0x36
	v_lshlrev_b32_e32 v5, 3, v0
	v_and_b32_e32 v15, 12, v0
	s_waitcnt vmcnt(13)
	v_and_b32_e32 v19, 64, v8
	v_lshlrev_b32_e32 v168, 4, v7
	v_bitop3_b32 v7, v3, v13, 12 bitop3:0x36
	v_cmp_gt_u32_e32 vcc, 32, v1
	v_bfe_u32 v14, v0, 1, 1
	v_and_b32_e32 v159, 8, v5
	v_or_b32_e32 v5, v3, v15
	v_xor_b32_e32 v18, 32, v8
	v_add_u32_e32 v19, 64, v19
	v_lshlrev_b32_e32 v169, 4, v7
	v_bitop3_b32 v7, v3, v13, 14 bitop3:0x36
	v_lshlrev_b32_e32 v132, 2, v3
	v_cndmask_b32_e64 v156, 0, 1.0, vcc
	v_cmp_lt_i32_e32 vcc, v18, v19
	v_lshlrev_b32_e32 v170, 4, v7
	v_bitop3_b32 v7, v16, v5, v14 bitop3:0x36
	v_cndmask_b32_e32 v8, v8, v18, vcc
	v_lshlrev_b32_e32 v171, 4, v7
	v_or_b32_e32 v7, v132, v11
	v_lshlrev_b32_e32 v160, 2, v8
	v_lshlrev_b32_e32 v8, 3, v10
	v_or_b32_e32 v10, 0x200, v0
	v_lshlrev_b32_e32 v172, 8, v7
	v_or3_b32 v7, v3, 2, v15
	v_or_b32_e32 v17, v16, v14
	v_lshrrev_b32_e32 v161, 4, v10
	v_bitop3_b32 v10, v16, v7, v14 bitop3:0x36
	v_readlane_b32 s1, v251, 28
	v_lshlrev_b32_e32 v173, 4, v10
	v_bitop3_b32 v10, v17, v5, 4 bitop3:0x36
	s_lshl_b32 s0, s1, 5
	v_readlane_b32 s4, v251, 27
	v_lshlrev_b32_e32 v174, 4, v10
	v_bitop3_b32 v10, v17, v7, 4 bitop3:0x36
	s_and_b32 s10, s0, 32
	s_lshl_b32 s0, s1, 10
	s_lshr_b32 s16, s4, 7
	v_lshlrev_b32_e32 v175, 4, v10
	v_bitop3_b32 v10, v17, v5, 8 bitop3:0x36
	v_bitop3_b32 v5, v17, v5, 12 bitop3:0x36
	v_and_b32_e32 v12, 31, v0
	s_add_i32 s11, s0, 0
	v_readlane_b32 s82, v251, 21
	v_readlane_b32 s83, v251, 22
	v_lshlrev_b32_e32 v178, 4, v5
	v_bitop3_b32 v5, v17, v7, 12 bitop3:0x36
	s_mul_i32 s0, s16, 0x600
	v_lshlrev_b32_e32 v4, 3, v3
	v_mov_b32_e32 v131, 0
	v_and_b32_e32 v130, 32, v1
	s_mov_b64 s[14:15], s[82:83]
	v_lshlrev_b32_e32 v179, 4, v5
	v_lshl_or_b32 v3, v3, 4, s0
	v_lshlrev_b32_e32 v5, 2, v12
	s_lshl_b32 s0, s4, 1
	v_lshl_add_u64 v[134:135], s[14:15], 0, v[130:131]
	v_lshlrev_b32_e32 v176, 4, v10
	v_bitop3_b32 v10, v17, v7, 8 bitop3:0x36
	v_lshlrev_b32_e32 v130, 4, v9
	v_sub_u32_e32 v3, v3, v5
	s_and_b32 s0, s0, 0x80
	v_lshlrev_b32_e32 v177, 4, v10
	v_lshl_add_u64 v[10:11], s[56:57], 0, v[130:131]
	s_mov_b64 s[2:3], 0x34b01000
	v_mov_b32_e32 v7, v131
	v_subrev_u32_e32 v3, s0, v3
	v_lshlrev_b32_e32 v2, 3, v9
	s_mov_b64 s[18:19], s[86:87]
	v_lshl_add_u64 v[136:137], v[10:11], 0, s[2:3]
	v_lshl_add_u64 v[6:7], s[56:57], 0, v[6:7]
	s_mov_b64 s[2:3], 0x34b01400
	v_add_u32_e32 v3, 0, v3
	s_mov_b32 s1, 0
	v_or_b32_e32 v155, s10, v12
	v_lshlrev_b32_e32 v158, 8, v12
	v_mov_b32_e32 v133, v131
	s_or_b32 s17, s10, 0x11f
	v_mov_b32_e32 v162, 0x2000
	v_or_b32_e32 v180, 0xffffffc0, v161
	s_lshl_b32 s18, s12, 6
	s_lshl_b32 s19, s13, 6
	v_lshl_add_u64 v[138:139], v[6:7], 0, s[2:3]
	v_or_b32_e32 v181, 0xffffffc0, v154
	v_add_u32_e32 v182, 0x10100, v3
	s_movk_i32 s20, 0x1800
	s_mov_b64 s[2:3], 0x1000
	v_lshlrev_b32_e32 v130, 1, v2
	v_lshlrev_b32_e32 v140, 1, v8
	s_mov_b64 s[4:5], 0x400
	s_add_i32 s21, s11, 0x4000
	s_add_i32 s26, s11, 0x6000
	v_lshlrev_b32_e32 v142, 1, v4
	v_mov_b32_e32 v183, 0x358637bd
	s_mov_b32 s27, 0x8000
	s_mov_b32 s28, 0xff61b1e6
	s_mov_b64 s[6:7], 0x60000
	s_mov_b32 s29, 0xc3e00000
	v_mov_b32_e32 v184, 0x80
	v_mov_b32_e32 v185, 0x1800
	v_mov_b32_e32 v186, 0x3000000
	v_mov_b32_e32 v187, 0x43e00000
	s_mov_b32 s30, s12
	v_readlane_b32 s73, v251, 12
	v_readlane_b32 s74, v251, 13
	v_readlane_b32 s75, v251, 14
	v_readlane_b32 s76, v251, 15
	v_readlane_b32 s77, v251, 16
	v_readlane_b32 s78, v251, 17
	v_readlane_b32 s79, v251, 18
	v_readlane_b32 s80, v251, 19
	v_readlane_b32 s81, v251, 20
	v_readfirstlane_b32 s98, v0
	s_nop 3
	s_and_b32 s98, s98, 0x3ff
	s_lshr_b32 s98, s98, 6
	s_cmp_ge_u32 s98, 4
	s_cbranch_scc0 .Lp4_prio_done
	s_setprio 1
.Lp4_prio_done:
	s_branch .LBB0_614
.LBB0_613:
	ds_bpermute_b32 v68, v160, v143
	v_lshlrev_b64 v[66:67], 11, v[144:145]
	v_lshl_add_u64 v[66:67], s[40:41], 0, v[66:67]
	v_lshl_add_u64 v[66:67], v[66:67], 0, s[8:9]
	s_add_i32 s30, s30, s13
	s_waitcnt lgkmcnt(0)
	v_add_f32_e32 v68, v143, v68
	v_div_scale_f32 v69, s[14:15], v68, v68, 1.0
	v_rcp_f32_e32 v70, v69
	v_div_scale_f32 v71, vcc, 1.0, v68, 1.0
	s_add_i32 s18, s18, s19
	v_fma_f32 v72, -v69, v70, 1.0
	v_fmac_f32_e32 v70, v72, v70
	v_mul_f32_e32 v72, v71, v70
	v_fma_f32 v73, -v69, v72, v71
	v_fmac_f32_e32 v72, v73, v70
	v_fma_f32 v69, -v69, v72, v71
	v_div_fmas_f32 v69, v69, v70, v72
	v_div_fixup_f32 v68, v69, v68, 1.0
	v_mul_f32_e32 v50, v68, v50
	v_mul_f32_e32 v51, v68, v51
	v_med3_f32 v50, v50, s29, v187
	v_med3_f32 v51, v51, s29, v187
	v_mov_b32_e32 v69, v131
	v_cvt_pk_fp8_f32 v69, v50, v51
	v_mul_f32_e32 v52, v68, v52
	v_mul_f32_e32 v50, v68, v53
	v_med3_f32 v51, v52, s29, v187
	v_med3_f32 v50, v50, s29, v187
	v_cvt_pk_fp8_f32 v69, v51, v50 op_sel:[0,0,1]
	v_mul_f32_e32 v50, v68, v54
	v_mul_f32_e32 v51, v68, v55
	v_med3_f32 v50, v50, s29, v187
	v_med3_f32 v51, v51, s29, v187
	v_mov_b32_e32 v53, v131
	v_cvt_pk_fp8_f32 v53, v50, v51
	v_mul_f32_e32 v52, v68, v56
	v_mul_f32_e32 v50, v68, v57
	v_med3_f32 v51, v52, s29, v187
	v_med3_f32 v50, v50, s29, v187
	v_cvt_pk_fp8_f32 v53, v51, v50 op_sel:[0,0,1]
	v_mul_f32_e32 v50, v68, v58
	v_mul_f32_e32 v51, v68, v59
	v_med3_f32 v50, v50, s29, v187
	v_med3_f32 v51, v51, s29, v187
	v_mov_b32_e32 v54, v131
	v_cvt_pk_fp8_f32 v54, v50, v51
	v_mul_f32_e32 v52, v68, v60
	v_mul_f32_e32 v50, v68, v61
	v_med3_f32 v51, v52, s29, v187
	v_med3_f32 v50, v50, s29, v187
	v_cvt_pk_fp8_f32 v54, v51, v50 op_sel:[0,0,1]
	v_lshl_add_u64 v[50:51], v[66:67], 0, v[132:133]
	global_store_dword v[50:51], v69, off
	global_store_dword v[50:51], v53, off offset:8
	global_store_dword v[50:51], v54, off offset:16
	v_mul_f32_e32 v52, v68, v62
	v_mul_f32_e32 v53, v68, v63
	v_med3_f32 v52, v52, s29, v187
	v_med3_f32 v53, v53, s29, v187
	v_mov_b32_e32 v55, v131
	v_cvt_pk_fp8_f32 v55, v52, v53
	v_mul_f32_e32 v54, v68, v64
	v_mul_f32_e32 v52, v68, v65
	v_med3_f32 v53, v54, s29, v187
	v_med3_f32 v52, v52, s29, v187
	v_mul_f32_e32 v34, v68, v34
	v_mul_f32_e32 v35, v68, v35
	v_cvt_pk_fp8_f32 v55, v53, v52 op_sel:[0,0,1]
	v_med3_f32 v34, v34, s29, v187
	v_med3_f32 v35, v35, s29, v187
	v_mov_b32_e32 v52, v131
	v_cvt_pk_fp8_f32 v52, v34, v35
	v_mul_f32_e32 v36, v68, v36
	v_mul_f32_e32 v34, v68, v37
	v_med3_f32 v35, v36, s29, v187
	v_med3_f32 v34, v34, s29, v187
	v_cvt_pk_fp8_f32 v52, v35, v34 op_sel:[0,0,1]
	v_mul_f32_e32 v34, v68, v38
	v_mul_f32_e32 v35, v68, v39
	v_med3_f32 v34, v34, s29, v187
	v_med3_f32 v35, v35, s29, v187
	v_mov_b32_e32 v37, v131
	v_cvt_pk_fp8_f32 v37, v34, v35
	v_mul_f32_e32 v36, v68, v40
	v_mul_f32_e32 v34, v68, v41
	v_med3_f32 v35, v36, s29, v187
	v_med3_f32 v34, v34, s29, v187
	v_cvt_pk_fp8_f32 v37, v35, v34 op_sel:[0,0,1]
	v_mul_f32_e32 v34, v68, v42
	v_mul_f32_e32 v35, v68, v43
	v_med3_f32 v34, v34, s29, v187
	v_med3_f32 v35, v35, s29, v187
	v_mov_b32_e32 v38, v131
	v_cvt_pk_fp8_f32 v38, v34, v35
	v_mul_f32_e32 v36, v68, v44
	v_mul_f32_e32 v34, v68, v45
	v_med3_f32 v35, v36, s29, v187
	v_med3_f32 v34, v34, s29, v187
	v_cvt_pk_fp8_f32 v38, v35, v34 op_sel:[0,0,1]
	v_mul_f32_e32 v34, v68, v46
	v_mul_f32_e32 v35, v68, v47
	global_store_dword v[50:51], v55, off offset:24
	global_store_dword v[50:51], v52, off offset:32
	global_store_dword v[50:51], v37, off offset:40
	global_store_dword v[50:51], v38, off offset:48
	v_med3_f32 v34, v34, s29, v187
	v_med3_f32 v35, v35, s29, v187
	v_mov_b32_e32 v37, v131
	v_cvt_pk_fp8_f32 v37, v34, v35
	v_mul_f32_e32 v36, v68, v48
	v_mul_f32_e32 v34, v68, v49
	v_med3_f32 v35, v36, s29, v187
	v_med3_f32 v34, v34, s29, v187
	v_mul_f32_e32 v18, v68, v18
	v_mul_f32_e32 v19, v68, v19
	v_cvt_pk_fp8_f32 v37, v35, v34 op_sel:[0,0,1]
	v_med3_f32 v18, v18, s29, v187
	v_med3_f32 v19, v19, s29, v187
	v_mov_b32_e32 v34, v131
	v_cvt_pk_fp8_f32 v34, v18, v19
	v_mul_f32_e32 v20, v68, v20
	v_mul_f32_e32 v18, v68, v21
	v_med3_f32 v19, v20, s29, v187
	v_med3_f32 v18, v18, s29, v187
	v_cvt_pk_fp8_f32 v34, v19, v18 op_sel:[0,0,1]
	v_mul_f32_e32 v18, v68, v22
	v_mul_f32_e32 v19, v68, v23
	v_med3_f32 v18, v18, s29, v187
	v_med3_f32 v19, v19, s29, v187
	v_mov_b32_e32 v21, v131
	v_cvt_pk_fp8_f32 v21, v18, v19
	v_mul_f32_e32 v20, v68, v24
	v_mul_f32_e32 v18, v68, v25
	v_med3_f32 v19, v20, s29, v187
	v_med3_f32 v18, v18, s29, v187
	v_cvt_pk_fp8_f32 v21, v19, v18 op_sel:[0,0,1]
	v_mul_f32_e32 v18, v68, v26
	v_mul_f32_e32 v19, v68, v27
	v_med3_f32 v18, v18, s29, v187
	v_med3_f32 v19, v19, s29, v187
	v_mov_b32_e32 v22, v131
	v_cvt_pk_fp8_f32 v22, v18, v19
	v_mul_f32_e32 v20, v68, v28
	v_mul_f32_e32 v18, v68, v29
	v_med3_f32 v19, v20, s29, v187
	v_med3_f32 v18, v18, s29, v187
	v_cvt_pk_fp8_f32 v22, v19, v18 op_sel:[0,0,1]
	v_mul_f32_e32 v18, v68, v30
	v_mul_f32_e32 v19, v68, v31
	global_store_dword v[50:51], v37, off offset:56
	global_store_dword v[50:51], v34, off offset:64
	global_store_dword v[50:51], v21, off offset:72
	global_store_dword v[50:51], v22, off offset:80
	v_med3_f32 v18, v18, s29, v187
	v_med3_f32 v19, v19, s29, v187
	v_mov_b32_e32 v21, v131
	v_cvt_pk_fp8_f32 v21, v18, v19
	v_mul_f32_e32 v20, v68, v32
	v_mul_f32_e32 v18, v68, v33
	v_med3_f32 v19, v20, s29, v187
	v_med3_f32 v18, v18, s29, v187
	v_mul_f32_e32 v2, v68, v2
	v_mul_f32_e32 v3, v68, v3
	v_cvt_pk_fp8_f32 v21, v19, v18 op_sel:[0,0,1]
	v_med3_f32 v2, v2, s29, v187
	v_med3_f32 v3, v3, s29, v187
	v_mov_b32_e32 v18, v131
	v_cvt_pk_fp8_f32 v18, v2, v3
	v_mul_f32_e32 v4, v68, v4
	v_mul_f32_e32 v2, v68, v5
	v_med3_f32 v3, v4, s29, v187
	v_med3_f32 v2, v2, s29, v187
	v_cvt_pk_fp8_f32 v18, v3, v2 op_sel:[0,0,1]
	v_mul_f32_e32 v2, v68, v6
	v_mul_f32_e32 v3, v68, v7
	v_med3_f32 v2, v2, s29, v187
	v_med3_f32 v3, v3, s29, v187
	v_mov_b32_e32 v5, v131
	v_cvt_pk_fp8_f32 v5, v2, v3
	v_mul_f32_e32 v4, v68, v8
	v_mul_f32_e32 v2, v68, v9
	v_med3_f32 v3, v4, s29, v187
	v_med3_f32 v2, v2, s29, v187
	v_cvt_pk_fp8_f32 v5, v3, v2 op_sel:[0,0,1]
	v_mul_f32_e32 v2, v68, v10
	v_mul_f32_e32 v3, v68, v11
	v_med3_f32 v2, v2, s29, v187
	v_med3_f32 v3, v3, s29, v187
	v_mov_b32_e32 v6, v131
	v_cvt_pk_fp8_f32 v6, v2, v3
	v_mul_f32_e32 v4, v68, v12
	v_mul_f32_e32 v2, v68, v13
	v_med3_f32 v3, v4, s29, v187
	v_med3_f32 v2, v2, s29, v187
	v_cvt_pk_fp8_f32 v6, v3, v2 op_sel:[0,0,1]
	v_mul_f32_e32 v2, v68, v14
	v_mul_f32_e32 v3, v68, v15
	global_store_dword v[50:51], v21, off offset:88
	global_store_dword v[50:51], v18, off offset:96
	global_store_dword v[50:51], v5, off offset:104
	global_store_dword v[50:51], v6, off offset:112
	v_med3_f32 v2, v2, s29, v187
	v_med3_f32 v3, v3, s29, v187
	v_mov_b32_e32 v5, v131
	v_cvt_pk_fp8_f32 v5, v2, v3
	v_mul_f32_e32 v4, v68, v16
	v_mul_f32_e32 v2, v68, v17
	v_med3_f32 v3, v4, s29, v187
	v_med3_f32 v2, v2, s29, v187
	v_cvt_pk_fp8_f32 v5, v3, v2 op_sel:[0,0,1]
	s_cmpk_gt_i32 s30, 0x3ff
	global_store_dword v[50:51], v5, off offset:120
	s_cbranch_scc1 .LBB0_630

.LBB0_630:
	s_setprio 0
	s_cmp_gt_i32 s59, 5
	s_cbranch_scc0 .LBB0_684
	s_waitcnt vmcnt(0)
	s_barrier
	s_mov_b64 s[0:1], exec
	v_readlane_b32 s2, v251, 9
	v_readlane_b32 s3, v251, 10
	s_and_b64 s[2:3], s[0:1], s[2:3]
	s_mov_b64 exec, s[2:3]
	s_cbranch_execz .LBB0_683
	s_add_i32 s2, 0, 0x21420
	v_mov_b32_e32 v2, s2
	s_waitcnt vmcnt(0) expcnt(0) lgkmcnt(0)
	ds_read_b32 v4, v2
	s_add_i32 s2, 0, 0x21424
	v_mov_b32_e32 v2, s2
	ds_read_b32 v2, v2
	s_waitcnt lgkmcnt(1)
	v_cmp_ne_u32_e32 vcc, 0, v4
	s_cbranch_vccnz .LBB0_647
	s_load_dwordx2 s[6:7], s[94:95], 0x4
	s_add_u32 s2, s56, 0x4200
	s_addc_u32 s3, s57, 0
	s_add_u32 s4, s56, 0x4400
	s_addc_u32 s5, s57, 0
	s_waitcnt lgkmcnt(0)
	s_mul_i32 s10, s6, s13
	s_add_u32 s6, s56, 0x4500
	s_mul_i32 s10, s10, s7
	s_addc_u32 s7, s57, 0
	s_add_u32 s8, s56, 0x4600
	s_addc_u32 s9, s57, 0
	s_add_u32 s14, s56, 0x4700
	s_addc_u32 s15, s57, 0
	s_add_u32 s22, s56, 0x4800
	s_addc_u32 s23, s57, 0
	s_add_u32 s26, s56, 0x4900
	s_addc_u32 s27, s57, 0
	s_add_u32 s28, s56, 0x4a00
	s_addc_u32 s29, s57, 0
	s_add_u32 s30, s56, 0x4b00
	s_addc_u32 s31, s57, 0
	s_add_u32 s42, s56, 0x4c00
	s_addc_u32 s43, s57, 0
	s_add_u32 s44, s56, 0x4d00
	s_addc_u32 s45, s57, 0
	s_add_u32 s46, s56, 0x4e00
	s_addc_u32 s47, s57, 0
	s_add_u32 s48, s56, 0x4f00
	s_addc_u32 s49, s57, 0
	s_add_u32 s50, s56, 0x5000
	s_addc_u32 s51, s57, 0
	s_add_u32 s52, s56, 0x5100
	s_addc_u32 s53, s57, 0
	s_add_u32 s64, s56, 0x5200
	s_addc_u32 s65, s57, 0
	s_add_u32 s66, s56, 0x5300
	s_addc_u32 s67, s57, 0
	s_mov_b32 s11, 1
	v_mov_b32_e32 v18, 0
	s_branch .LBB0_635
